# baseline (speedup 1.0000x reference)
_Z11init_kernelPKfS0_S0_S0_PDF16_S1_:
	s_load_dwordx8 s[4:11], s[0:1], 0x0
	s_load_dwordx4 s[12:15], s[0:1], 0x20
	v_readfirstlane_b32 s3, v0
	v_bfe_u32 v32, v0, 4, 2
	v_and_b32_e32 v33, 15, v0
	s_lshr_b32 s3, s3, 6
	s_lshl_b32 s17, s2, 11
	s_lshl_b32 s18, s2, 8
	s_lshl_b32 s19, s3, 7
	s_lshl_b32 s20, s3, 6
	v_mul_u32_u24_e32 v34, 36, v32
	v_lshl_or_b32 v34, v33, 7, v34
	v_mul_u32_u24_e32 v35, 0x900, v32
	v_lshl_or_b32 v35, v33, 2, v35
	v_lshlrev_b32_e32 v36, 2, v33
	v_lshlrev_b32_e32 v37, 4, v0
	v_lshlrev_b32_e32 v42, 9, v32
	v_lshl_or_b32 v42, v33, 1, v42
	v_mov_b32_e32 v44, 0
	v_mov_b32_e32 v45, 0
	v_mov_b32_e32 v46, 0
	v_mov_b32_e32 v47, 0
	v_mov_b32_e32 v39, 0
	v_mov_b32_e32 v41, 0
	v_add_u32_e32 v38, 20, v34
	v_lshlrev_b32_e32 v40, 4, v33
	v_cmp_eq_u32_e32 vcc, 3, v32
	s_waitcnt lgkmcnt(0)
	s_add_u32 s4, s4, s17
	s_addc_u32 s5, s5, 0
	s_add_u32 s6, s6, s18
	s_addc_u32 s7, s7, 0
	s_add_u32 s8, s8, s19
	s_addc_u32 s9, s9, 0
	v_lshl_add_u64 v[38:39], s[4:5], 0, v[38:39]
	v_lshl_add_u64 v[40:41], s[6:7], 0, v[40:41]
	v_cndmask_b32_e32 v38, v38, v40, vcc
	v_cndmask_b32_e32 v39, v39, v41, vcc
	global_load_dwordx4 v[2:5], v34, s[4:5] nt
	global_load_dword v6, v34, s[4:5] offset:16 nt
	global_load_dwordx4 v[8:11], v[38:39], off nt
	global_load_dword v12, v35, s[8:9]
	global_load_dword v21, v35, s[8:9] offset:64
	global_load_dword v13, v35, s[8:9] offset:256
	global_load_dword v22, v35, s[8:9] offset:320
	global_load_dword v14, v35, s[8:9] offset:512
	global_load_dword v23, v35, s[8:9] offset:576
	global_load_dword v15, v35, s[8:9] offset:768
	global_load_dword v24, v35, s[8:9] offset:832
	global_load_dword v16, v35, s[8:9] offset:1024
	global_load_dword v25, v35, s[8:9] offset:1088
	global_load_dword v17, v35, s[8:9] offset:1280
	global_load_dword v26, v35, s[8:9] offset:1344
	global_load_dword v18, v35, s[8:9] offset:1536
	global_load_dword v27, v35, s[8:9] offset:1600
	global_load_dword v19, v35, s[8:9] offset:1792
	global_load_dword v28, v35, s[8:9] offset:1856
	global_load_dword v20, v35, s[8:9] offset:2048
	global_load_dword v29, v35, s[8:9] offset:2112
	s_add_u32 s10, s10, s19
	s_addc_u32 s11, s11, 0
	global_load_dword v30, v36, s[10:11]
	global_load_dword v31, v36, s[10:11] offset:64
	s_add_u32 s14, s14, s17
	s_addc_u32 s15, s15, 0
	global_store_dwordx4 v37, v[44:47], s[14:15]
	s_add_u32 s12, s12, s17
	s_addc_u32 s13, s13, 0
	s_add_u32 s12, s12, s20
	s_addc_u32 s13, s13, 0
	v_accvgpr_write_b32 a0, 0
	v_accvgpr_write_b32 a1, 0
	v_accvgpr_write_b32 a2, 0
	v_accvgpr_write_b32 a3, 0
	v_accvgpr_write_b32 a4, 0
	v_accvgpr_write_b32 a5, 0
	v_accvgpr_write_b32 a6, 0
	v_accvgpr_write_b32 a7, 0
	v_and_b32_e32 v43, 1, v0
	s_waitcnt vmcnt(21)
	s_waitcnt vmcnt(19)
	v_mfma_f32_16x16x4_f32 a[0:3], v2, v12, a[0:3]
	v_mfma_f32_16x16x4_f32 a[4:7], v2, v21, a[4:7]
	s_waitcnt vmcnt(17)
	v_mfma_f32_16x16x4_f32 a[0:3], v3, v13, a[0:3]
	v_mfma_f32_16x16x4_f32 a[4:7], v3, v22, a[4:7]
	s_waitcnt vmcnt(15)
	v_mfma_f32_16x16x4_f32 a[0:3], v4, v14, a[0:3]
	v_mfma_f32_16x16x4_f32 a[4:7], v4, v23, a[4:7]
	s_waitcnt vmcnt(13)
	v_mfma_f32_16x16x4_f32 a[0:3], v5, v15, a[0:3]
	v_mfma_f32_16x16x4_f32 a[4:7], v5, v24, a[4:7]
	s_waitcnt vmcnt(11)
	v_mfma_f32_16x16x4_f32 a[0:3], v6, v16, a[0:3]
	v_mfma_f32_16x16x4_f32 a[4:7], v6, v25, a[4:7]
	s_waitcnt vmcnt(9)
	v_mfma_f32_16x16x4_f32 a[0:3], v8, v17, a[0:3]
	v_mfma_f32_16x16x4_f32 a[4:7], v8, v26, a[4:7]
	s_waitcnt vmcnt(7)
	v_mfma_f32_16x16x4_f32 a[0:3], v9, v18, a[0:3]
	v_mfma_f32_16x16x4_f32 a[4:7], v9, v27, a[4:7]
	s_waitcnt vmcnt(5)
	v_mfma_f32_16x16x4_f32 a[0:3], v10, v19, a[0:3]
	v_mfma_f32_16x16x4_f32 a[4:7], v10, v28, a[4:7]
	s_waitcnt vmcnt(3)
	v_mfma_f32_16x16x4_f32 a[0:3], v11, v20, a[0:3]
	v_mfma_f32_16x16x4_f32 a[4:7], v11, v29, a[4:7]
	v_cmp_eq_u32_e32 vcc, 0, v43
	s_waitcnt vmcnt(1)
	s_nop 7
	v_accvgpr_read_b32 v2, a0
	v_accvgpr_read_b32 v3, a1
	v_accvgpr_read_b32 v4, a2
	v_accvgpr_read_b32 v5, a3
	v_accvgpr_read_b32 v6, a4
	v_accvgpr_read_b32 v7, a5
	v_accvgpr_read_b32 v8, a6
	v_accvgpr_read_b32 v9, a7
	v_add_f32_e32 v2, v30, v2
	v_add_f32_e32 v3, v30, v3
	v_add_f32_e32 v4, v30, v4
	v_add_f32_e32 v5, v30, v5
	v_add_f32_e32 v6, v31, v6
	v_add_f32_e32 v7, v31, v7
	v_add_f32_e32 v8, v31, v8
	v_add_f32_e32 v9, v31, v9
	v_mov_b32_dpp v50, v2 quad_perm:[1,0,3,2] row_mask:0xf bank_mask:0xf
	v_mov_b32_dpp v51, v3 quad_perm:[1,0,3,2] row_mask:0xf bank_mask:0xf
	v_mov_b32_dpp v52, v4 quad_perm:[1,0,3,2] row_mask:0xf bank_mask:0xf
	v_mov_b32_dpp v53, v5 quad_perm:[1,0,3,2] row_mask:0xf bank_mask:0xf
	v_mov_b32_dpp v54, v6 quad_perm:[1,0,3,2] row_mask:0xf bank_mask:0xf
	v_mov_b32_dpp v55, v7 quad_perm:[1,0,3,2] row_mask:0xf bank_mask:0xf
	v_mov_b32_dpp v56, v8 quad_perm:[1,0,3,2] row_mask:0xf bank_mask:0xf
	v_mov_b32_dpp v57, v9 quad_perm:[1,0,3,2] row_mask:0xf bank_mask:0xf
	v_cvt_pk_f16_f32 v2, v2, v50
	v_cvt_pk_f16_f32 v3, v3, v51
	v_cvt_pk_f16_f32 v4, v4, v52
	v_cvt_pk_f16_f32 v5, v5, v53
	v_cvt_pk_f16_f32 v6, v6, v54
	v_cvt_pk_f16_f32 v7, v7, v55
	v_cvt_pk_f16_f32 v8, v8, v56
	v_cvt_pk_f16_f32 v9, v9, v57
	s_and_saveexec_b64 s[2:3], vcc
	global_store_dword v42, v2, s[12:13]
	global_store_dword v42, v6, s[12:13] offset:32
	global_store_dword v42, v3, s[12:13] offset:128
	global_store_dword v42, v7, s[12:13] offset:160
	global_store_dword v42, v4, s[12:13] offset:256
	global_store_dword v42, v8, s[12:13] offset:288
	global_store_dword v42, v5, s[12:13] offset:384
	global_store_dword v42, v9, s[12:13] offset:416
	s_endpgm
	.p2align	8

	.amdhsa_kernel _Z11init_kernelPKfS0_S0_S0_PDF16_S1_
		.amdhsa_group_segment_fixed_size 4224
		.amdhsa_private_segment_fixed_size 0
		.amdhsa_kernarg_size 48
		.amdhsa_user_sgpr_count 2
		.amdhsa_user_sgpr_dispatch_ptr 0
		.amdhsa_user_sgpr_queue_ptr 0
		.amdhsa_user_sgpr_kernarg_segment_ptr 1
		.amdhsa_user_sgpr_dispatch_id 0
		.amdhsa_user_sgpr_kernarg_preload_length 0
		.amdhsa_user_sgpr_kernarg_preload_offset 0
		.amdhsa_user_sgpr_private_segment_size 0
		.amdhsa_uses_dynamic_stack 0
		.amdhsa_enable_private_segment 0
		.amdhsa_system_sgpr_workgroup_id_x 1
		.amdhsa_system_sgpr_workgroup_id_y 0
		.amdhsa_system_sgpr_workgroup_id_z 0
		.amdhsa_system_sgpr_workgroup_info 0
		.amdhsa_system_vgpr_workitem_id 0
		.amdhsa_next_free_vgpr 68
		.amdhsa_next_free_sgpr 24
		.amdhsa_accum_offset 60
		.amdhsa_reserve_vcc 1
		.amdhsa_float_round_mode_32 0
		.amdhsa_float_round_mode_16_64 0
		.amdhsa_float_denorm_mode_32 3
		.amdhsa_float_denorm_mode_16_64 3
		.amdhsa_dx10_clamp 1
		.amdhsa_ieee_mode 1
		.amdhsa_fp16_overflow 0
		.amdhsa_tg_split 0
		.amdhsa_exception_fp_ieee_invalid_op 0
		.amdhsa_exception_fp_denorm_src 0
		.amdhsa_exception_fp_ieee_div_zero 0
		.amdhsa_exception_fp_ieee_overflow 0
		.amdhsa_exception_fp_ieee_underflow 0
		.amdhsa_exception_fp_ieee_inexact 0
		.amdhsa_exception_int_div_zero 0
	.end_amdhsa_kernel

amdhsa.kernels:
  - .agpr_count:     8
    .args:
      - .actual_access:  read_only
        .address_space:  global
        .offset:         0
        .size:           8
        .value_kind:     global_buffer
      - .actual_access:  read_only
        .address_space:  global
        .offset:         8
        .size:           8
        .value_kind:     global_buffer
      - .actual_access:  read_only
        .address_space:  global
        .offset:         16
        .size:           8
        .value_kind:     global_buffer
      - .actual_access:  read_only
        .address_space:  global
        .offset:         24
        .size:           8
        .value_kind:     global_buffer
      - .actual_access:  write_only
        .address_space:  global
        .offset:         32
        .size:           8
        .value_kind:     global_buffer
      - .actual_access:  write_only
        .address_space:  global
        .offset:         40
        .size:           8
        .value_kind:     global_buffer
    .group_segment_fixed_size: 4224
    .kernarg_segment_align: 8
    .kernarg_segment_size: 48
    .language:       OpenCL C
    .language_version:
      - 2
      - 0
    .max_flat_workgroup_size: 128
    .name:           _Z11init_kernelPKfS0_S0_S0_PDF16_S1_
    .private_segment_fixed_size: 0
    .sgpr_count:     30
    .sgpr_spill_count: 0
    .symbol:         _Z11init_kernelPKfS0_S0_S0_PDF16_S1_.kd
    .uniform_work_group_size: 1
    .uses_dynamic_stack: false
    .vgpr_count:     68
    .vgpr_spill_count: 0
    .wavefront_size: 64
  - .agpr_count:     8
    .args:
      - .actual_access:  read_only
        .address_space:  global
        .offset:         0
        .size:           8
        .value_kind:     global_buffer
      - .actual_access:  read_only
        .address_space:  global
        .offset:         8
        .size:           8
        .value_kind:     global_buffer
      - .actual_access:  read_only
        .address_space:  global
        .offset:         16
        .size:           8
        .value_kind:     global_buffer
      - .actual_access:  read_only
        .address_space:  global
        .offset:         24
        .size:           8
        .value_kind:     global_buffer
      - .actual_access:  read_only
        .address_space:  global
        .offset:         32
        .size:           8
        .value_kind:     global_buffer
      - .actual_access:  read_only
        .address_space:  global
        .offset:         40
        .size:           8
        .value_kind:     global_buffer
      - .actual_access:  write_only
        .address_space:  global
        .offset:         48
        .size:           8
        .value_kind:     global_buffer
    .group_segment_fixed_size: 4352
    .kernarg_segment_align: 8
    .kernarg_segment_size: 56
    .language:       OpenCL C
    .language_version:
      - 2
      - 0
    .max_flat_workgroup_size: 128
    .name:           _Z12final_kernelPKDF16_S0_PKfS2_S2_S2_Pf
    .private_segment_fixed_size: 0
    .sgpr_count:     30
    .sgpr_spill_count: 0
    .symbol:         _Z12final_kernelPKDF16_S0_PKfS2_S2_S2_Pf.kd
    .uniform_work_group_size: 1
    .uses_dynamic_stack: false
    .vgpr_count:     88
    .vgpr_spill_count: 0
    .wavefront_size: 64
  - .agpr_count:     0
    .args:
      - .actual_access:  read_only
        .address_space:  global
        .offset:         0
        .size:           8
        .value_kind:     global_buffer
      - .actual_access:  read_only
        .address_space:  global
        .offset:         8
        .size:           8
        .value_kind:     global_buffer
      - .actual_access:  read_only
        .address_space:  global
        .offset:         16
        .size:           8
        .value_kind:     global_buffer
      - .actual_access:  read_only
        .address_space:  global
        .offset:         24
        .size:           8
        .value_kind:     global_buffer
      - .actual_access:  read_only
        .address_space:  global
        .offset:         32
        .size:           8
        .value_kind:     global_buffer
      - .actual_access:  read_only
        .address_space:  global
        .offset:         40
        .size:           8
        .value_kind:     global_buffer
      - .actual_access:  read_only
        .address_space:  global
        .offset:         48
        .size:           8
        .value_kind:     global_buffer
      - .actual_access:  read_only
        .address_space:  global
        .offset:         56
        .size:           8
        .value_kind:     global_buffer
      - .actual_access:  read_only
        .address_space:  global
        .offset:         64
        .size:           8
        .value_kind:     global_buffer
      - .actual_access:  read_only
        .address_space:  global
        .offset:         72
        .size:           8
        .value_kind:     global_buffer
      - .address_space:  global
        .offset:         80
        .size:           8
        .value_kind:     global_buffer
    .group_segment_fixed_size: 16896
    .kernarg_segment_align: 8
    .kernarg_segment_size: 88
    .language:       OpenCL C
    .language_version:
      - 2
      - 0
    .max_flat_workgroup_size: 128
    .name:           _Z11edge_kernelILi36ELb1EEvPKfS1_PKDF16_PKiS5_S1_S1_S1_S1_S1_PDF16_
    .private_segment_fixed_size: 0
    .sgpr_count:     45
    .sgpr_spill_count: 0
    .symbol:         _Z11edge_kernelILi36ELb1EEvPKfS1_PKDF16_PKiS5_S1_S1_S1_S1_S1_PDF16_.kd
    .uniform_work_group_size: 1
    .uses_dynamic_stack: false
    .vgpr_count:     168
    .vgpr_spill_count: 0
    .wavefront_size: 64
  - .agpr_count:     0
    .args:
      - .actual_access:  read_only
        .address_space:  global
        .offset:         0
        .size:           8
        .value_kind:     global_buffer
      - .actual_access:  read_only
        .address_space:  global
        .offset:         8
        .size:           8
        .value_kind:     global_buffer
      - .actual_access:  read_only
        .address_space:  global
        .offset:         16
        .size:           8
        .value_kind:     global_buffer
      - .actual_access:  read_only
        .address_space:  global
        .offset:         24
        .size:           8
        .value_kind:     global_buffer
      - .actual_access:  read_only
        .address_space:  global
        .offset:         32
        .size:           8
        .value_kind:     global_buffer
      - .actual_access:  read_only
        .address_space:  global
        .offset:         40
        .size:           8
        .value_kind:     global_buffer
      - .actual_access:  read_only
        .address_space:  global
        .offset:         48
        .size:           8
        .value_kind:     global_buffer
      - .actual_access:  read_only
        .address_space:  global
        .offset:         56
        .size:           8
        .value_kind:     global_buffer
      - .actual_access:  read_only
        .address_space:  global
        .offset:         64
        .size:           8
        .value_kind:     global_buffer
      - .actual_access:  read_only
        .address_space:  global
        .offset:         72
        .size:           8
        .value_kind:     global_buffer
      - .address_space:  global
        .offset:         80
        .size:           8
        .value_kind:     global_buffer
    .group_segment_fixed_size: 16896
    .kernarg_segment_align: 8
    .kernarg_segment_size: 88
    .language:       OpenCL C
    .language_version:
      - 2
      - 0
    .max_flat_workgroup_size: 128
    .name:           _Z11edge_kernelILi64ELb0EEvPKfS1_PKDF16_PKiS5_S1_S1_S1_S1_S1_PDF16_
    .private_segment_fixed_size: 0
    .sgpr_count:     44
    .sgpr_spill_count: 0
    .symbol:         _Z11edge_kernelILi64ELb0EEvPKfS1_PKDF16_PKiS5_S1_S1_S1_S1_S1_PDF16_.kd
    .uniform_work_group_size: 1
    .uses_dynamic_stack: false
    .vgpr_count:     168
    .vgpr_spill_count: 0
    .wavefront_size: 64
